# grid barrier: last XCD leader bumps all per-XCD generation words directly, other leaders poll their own XCD word (one cross-chip hop less)
# speedup vs baseline: 1.0376x; 1.0041x over previous
.LBB0_1098:
	s_or_b64 exec, exec, s[36:37]
	v_cvt_f32_u32_e32 v4, v0
	s_waitcnt vmcnt(0)
	v_readfirstlane_b32 s6, v3
	s_add_u32 s36, s0, 0x7500
	s_addc_u32 s37, s1, 0
	v_rcp_iflag_f32_e32 v4, v4
	v_add_u32_e32 v2, s6, v2
	s_mov_b64 s[38:39], -1
	buffer_inv sc1
	v_mul_f32_e32 v3, 0x4f7ffffe, v4
	v_cvt_u32_f32_e32 v3, v3
	v_sub_u32_e32 v4, 0, v0
	v_mul_lo_u32 v4, v4, v3
	v_mul_hi_u32 v4, v3, v4
	v_add_u32_e32 v3, v3, v4
	v_mul_hi_u32 v3, v2, v3
	v_mul_lo_u32 v4, v3, v0
	v_sub_u32_e32 v4, v2, v4
	v_add_u32_e32 v5, 1, v3
	v_cmp_ge_u32_e32 vcc, v4, v0
	v_add_u32_e32 v2, 1, v2
	s_nop 0
	v_cndmask_b32_e32 v3, v3, v5, vcc
	v_sub_u32_e32 v5, v4, v0
	v_cndmask_b32_e32 v4, v4, v5, vcc
	v_add_u32_e32 v5, 1, v3
	v_cmp_ge_u32_e32 vcc, v4, v0
	s_nop 1
	v_cndmask_b32_e32 v4, v3, v5, vcc
	v_mul_lo_u32 v3, v0, v4
	v_add_u32_e32 v0, v3, v0
	v_cmp_ne_u32_e32 vcc, v2, v0
	s_and_b32 s101, vcc_lo, 1
	v_mov_b32_e32 v5, 0x2400
	v_mov_b64_e32 v[2:3], s[36:37]
	s_and_saveexec_b64 s[30:31], vcc
	s_cbranch_execz .LBB0_1110
	global_load_dword v0, v5, s[26:27] sc1
	s_mov_b64 s[42:43], 0
	s_waitcnt vmcnt(0)
	v_cmp_eq_u32_e32 vcc, v0, v4
	s_and_saveexec_b64 s[40:41], vcc
	s_cbranch_execz .LBB0_1109
	s_add_u32 s38, s0, 0x4200
	s_addc_u32 s39, s1, 0
	s_mov_b32 s6, 1
	s_mov_b64 s[0:1], 0
	s_branch .LBB0_1102

.LBB0_1104:
	global_load_dword v0, v5, s[26:27] sc1
	s_add_i32 s6, s6, 1
	s_mov_b64 s[46:47], -1
	s_waitcnt vmcnt(0)
	v_cmp_ne_u32_e32 vcc, v0, v4
	s_orn2_b64 s[44:45], vcc, exec
	s_branch .LBB0_1101

.LBB0_1110:
	s_or_b64 exec, exec, s[30:31]
	s_cmp_lg_u32 s101, 0
	s_cbranch_scc1 .Lb2_a
	s_mov_b64 s[38:39], 0
.Lb2_a:
	s_and_saveexec_b64 s[0:1], s[38:39]
	s_cbranch_execz .LBB0_1112
	global_atomic_add v[2:3], v225, off
.LBB0_1112:
	s_or_b64 exec, exec, s[0:1]
	s_waitcnt vmcnt(0)
	s_cmp_lg_u32 s101, 0
	s_cbranch_scc1 .Lb2_skip
	v_readlane_b32 s6, v254, 27
	s_sub_u32 s44, s26, s6
	s_subb_u32 s45, s27, 0
	s_add_u32 s44, s44, 0x2400
	s_addc_u32 s45, s45, 0
	global_atomic_add v1, v225, s[44:45]
	global_atomic_add v1, v225, s[44:45] offset:256
	global_atomic_add v1, v225, s[44:45] offset:512
	global_atomic_add v1, v225, s[44:45] offset:768
	global_atomic_add v1, v225, s[44:45] offset:1024
	global_atomic_add v1, v225, s[44:45] offset:1280
	global_atomic_add v1, v225, s[44:45] offset:1536
	global_atomic_add v1, v225, s[44:45] offset:1792
	global_atomic_add v1, v225, s[44:45] offset:2048
	global_atomic_add v1, v225, s[44:45] offset:2304
	global_atomic_add v1, v225, s[44:45] offset:2560
	global_atomic_add v1, v225, s[44:45] offset:2816
	global_atomic_add v1, v225, s[44:45] offset:3072
	global_atomic_add v1, v225, s[44:45] offset:3328
	global_atomic_add v1, v225, s[44:45] offset:3584
	global_atomic_add v1, v225, s[44:45] offset:3840
.Lb2_skip:
	s_waitcnt vmcnt(0)
.LBB0_1113:
	s_or_b64 exec, exec, s[4:5]
	s_mov_b64 s[4:5], 0
	s_waitcnt lgkmcnt(0)
	s_barrier
